# cache policy: nt also on the w_out epilogue's once-read residual loads
# baseline (speedup 1.0000x reference)
; __device__ __forceinline__ unsigned cvt_pk_bf16(float lo, float hi) { unsigned r; asm volatile("v_cvt_pk_bf16_f32 %0, %1, %2" : "=v"(r) : "v"(lo), "v"(hi)); return r; }
;     __device__ __forceinline__ void operator()(const f32x4 (&acc)[2][2][4][2], const Unit& u, int wr, int wc, int fr, int fq) const {
;         const int row0 = u.pm * BM + wr * 64 + fr, col0 = u.pn * BM + wc * 32 + 8 * fq;
;         const float* ga = mod + (size_t)modrow_of(u.pm * BM) * 12288 + 2 * D;
;         constexpr float sc = WOUT_F8 ? 1.f / 32.f : 1.f;
;         f32x4 gv[2][2];
; #pragma unroll
;         for (int bj = 0; bj < 2; ++bj)
; #pragma unroll
;             for (int n = 0; n < 2; ++n) gv[bj][n] = *(const f32x4*)(ga + col0 + bj * HALF + n * 4) * sc;
;         if (resb) {
; #pragma unroll
;             for (int ai = 0; ai < 2; ++ai)
; #pragma unroll
;                 for (int m = 0; m < 4; ++m) { const int row = row0 + ai * HALF + m * 16; const bf16_t* rp = resb + (size_t)row * D + col0; bf16_t* xp = X + (size_t)row * D + col0;
; #pragma unroll
;                     for (int bj = 0; bj < 2; ++bj) { const u32x4 r = *(const u32x4*)(rp + bj * HALF);
;                         const f32x4 v0 = (f32x4){bflo(r.x), bfhi(r.x), bflo(r.y), bfhi(r.y)} + gv[bj][0] * acc[ai][bj][m][0], v1 = (f32x4){bflo(r.z), bfhi(r.z), bflo(r.w), bfhi(r.w)} + gv[bj][1] * acc[ai][bj][m][1];
;                         u32x4 o; o.x = cvt_pk_bf16(v0[0], v0[1]); o.y = cvt_pk_bf16(v0[2], v0[3]); o.z = cvt_pk_bf16(v1[0], v1[1]); o.w = cvt_pk_bf16(v1[2], v1[3]);
;                         *(u32x4*)(xp + bj * HALF) = o; } }
.LBB0_923:
	s_lshl_b32 s37, s54, 8
	s_min_i32 s34, s37, 0x4000
	s_ashr_i32 s34, s34, 11
	s_mul_hi_i32 s35, s34, 0xc000
	s_mul_i32 s34, s34, 0xc000
	v_lshl_or_b32 v6, s52, 8, v181
	s_add_u32 s34, s74, s34
	s_addc_u32 s35, s75, s35
	v_ashrrev_i32_e32 v7, 31, v6
	v_lshl_add_u64 v[8:9], v[6:7], 2, s[34:35]
	s_mov_b32 s34, 0x104000
	v_add_co_u32_e32 v2, vcc, s34, v8
	s_mov_b64 s[34:35], 0x104000
	s_nop 15
	s_nop 15
	s_nop 0
	v_addc_co_u32_e32 v3, vcc, 0, v9, vcc
	v_lshl_add_u64 v[12:13], v[8:9], 0, s[34:35]
	global_load_dwordx4 v[2:5], v[2:3], off
	s_nop 0
	global_load_dwordx4 v[8:11], v[12:13], off offset:16
	global_load_dwordx4 v[170:173], v[12:13], off offset:512
	global_load_dwordx4 v[174:177], v[12:13], off offset:528
	v_readlane_b32 s56, v254, 32
	v_add_u32_e32 v24, s37, v178
	v_readlane_b32 s57, v254, 33
	s_mov_b64 s[34:35], -1
	v_or_b32_e32 v30, 16, v24
	v_or_b32_e32 v28, 32, v24
	s_andn2_b64 vcc, exec, s[56:57]
	v_or_b32_e32 v26, 48, v24
	s_waitcnt vmcnt(0)
	v_pk_mul_f32 v[16:17], v[10:11], s[20:21] op_sel_hi:[1,0]
	v_pk_mul_f32 v[20:21], v[4:5], s[20:21] op_sel_hi:[1,0]
	v_pk_mul_f32 v[22:23], v[2:3], s[20:21] op_sel_hi:[1,0]
	v_pk_mul_f32 v[18:19], v[8:9], s[20:21] op_sel_hi:[1,0]
	v_pk_mul_f32 v[12:13], v[172:173], s[20:21] op_sel_hi:[1,0]
	v_pk_mul_f32 v[14:15], v[170:171], s[20:21] op_sel_hi:[1,0]
	v_pk_mul_f32 v[8:9], v[176:177], s[20:21] op_sel_hi:[1,0]
	v_pk_mul_f32 v[10:11], v[174:175], s[20:21] op_sel_hi:[1,0]
	s_cbranch_vccnz .LBB0_925
	v_ashrrev_i32_e32 v25, 31, v24
	v_lshlrev_b64 v[186:187], 12, v[24:25]
	v_lshl_add_u64 v[32:33], s[38:39], 0, v[186:187]
	v_lshl_add_u64 v[32:33], v[6:7], 1, v[32:33]
	global_load_dwordx4 v[190:193], v[32:33], off nt
	global_load_dwordx4 v[196:199], v[32:33], off offset:256 nt
	s_mov_b64 s[34:35], 0x10000
	v_lshl_add_u64 v[184:185], v[32:33], 0, s[34:35]
	global_load_dwordx4 v[200:203], v[184:185], off nt
	global_load_dwordx4 v[204:207], v[184:185], off offset:256 nt
	s_mov_b64 s[34:35], 0x20000
	v_lshl_add_u64 v[184:185], v[32:33], 0, s[34:35]
	global_load_dwordx4 v[208:211], v[184:185], off nt
	global_load_dwordx4 v[212:215], v[184:185], off offset:256 nt
	s_mov_b64 s[34:35], 0x30000
	v_lshl_add_u64 v[184:185], v[32:33], 0, s[34:35]
	global_load_dwordx4 v[216:219], v[184:185], off nt
	global_load_dwordx4 v[220:223], v[184:185], off offset:256 nt
	s_mov_b64 s[34:35], 0x80000
	v_lshl_add_u64 v[184:185], v[32:33], 0, s[34:35]
	global_load_dwordx4 v[242:245], v[184:185], off nt
	global_load_dwordx4 v[246:249], v[184:185], off offset:256 nt
	s_waitcnt vmcnt(9)
	v_lshlrev_b32_e32 v170, 16, v190
	v_and_b32_e32 v171, 0xffff0000, v190
	v_lshlrev_b32_e32 v172, 16, v191
	v_and_b32_e32 v173, 0xffff0000, v191
	v_lshlrev_b32_e32 v174, 16, v192
	v_and_b32_e32 v175, 0xffff0000, v192
	v_lshlrev_b32_e32 v176, 16, v193
	v_and_b32_e32 v177, 0xffff0000, v193
	v_pk_fma_f32 v[170:171], v[158:159], v[22:23], v[170:171]
	v_pk_fma_f32 v[172:173], v[160:161], v[20:21], v[172:173]
	v_pk_fma_f32 v[174:175], v[154:155], v[18:19], v[174:175]
	v_pk_fma_f32 v[176:177], v[156:157], v[16:17], v[176:177]
	v_cvt_pk_bf16_f32 v170, v170, v171
	v_cvt_pk_bf16_f32 v171, v172, v173
	v_cvt_pk_bf16_f32 v172, v174, v175
	v_cvt_pk_bf16_f32 v173, v176, v177
	global_store_dwordx4 v[32:33], v[170:173], off
	s_nop 1
	s_mov_b64 s[34:35], 0x90000
	v_lshl_add_u64 v[184:185], v[32:33], 0, s[34:35]
	global_load_dwordx4 v[190:193], v[184:185], off nt
	global_load_dwordx4 v[158:161], v[184:185], off offset:256 nt
	s_mov_b64 s[34:35], 0xa0000
	v_lshl_add_u64 v[184:185], v[32:33], 0, s[34:35]
	global_load_dwordx4 v[154:157], v[184:185], off nt
	s_waitcnt vmcnt(12)
	v_lshlrev_b32_e32 v170, 16, v196
	v_and_b32_e32 v171, 0xffff0000, v196
	v_lshlrev_b32_e32 v172, 16, v197
	v_and_b32_e32 v173, 0xffff0000, v197
	v_lshlrev_b32_e32 v174, 16, v198
	v_and_b32_e32 v175, 0xffff0000, v198
	v_lshlrev_b32_e32 v176, 16, v199
	v_and_b32_e32 v177, 0xffff0000, v199
	v_pk_fma_f32 v[170:171], v[150:151], v[14:15], v[170:171]
	v_pk_fma_f32 v[172:173], v[152:153], v[12:13], v[172:173]
	v_pk_fma_f32 v[174:175], v[146:147], v[10:11], v[174:175]
	v_pk_fma_f32 v[176:177], v[148:149], v[8:9], v[176:177]
	v_cvt_pk_bf16_f32 v170, v170, v171
	v_cvt_pk_bf16_f32 v171, v172, v173
	v_cvt_pk_bf16_f32 v172, v174, v175
	v_cvt_pk_bf16_f32 v173, v176, v177
	global_store_dwordx4 v[32:33], v[170:173], off offset:256
	s_nop 1
	global_load_dwordx4 v[196:199], v[184:185], off offset:256 nt
	s_mov_b64 s[34:35], 0xb0000
	v_lshl_add_u64 v[184:185], v[32:33], 0, s[34:35]
	global_load_dwordx4 v[150:153], v[184:185], off nt
	global_load_dwordx4 v[146:149], v[184:185], off offset:256 nt
	s_waitcnt vmcnt(15)
	v_lshlrev_b32_e32 v170, 16, v200
	v_and_b32_e32 v171, 0xffff0000, v200
	v_lshlrev_b32_e32 v172, 16, v201
	v_and_b32_e32 v173, 0xffff0000, v201
	v_lshlrev_b32_e32 v174, 16, v202
	v_and_b32_e32 v175, 0xffff0000, v202
	v_lshlrev_b32_e32 v176, 16, v203
	v_and_b32_e32 v177, 0xffff0000, v203
	v_pk_fma_f32 v[170:171], v[142:143], v[22:23], v[170:171]
	v_pk_fma_f32 v[172:173], v[144:145], v[20:21], v[172:173]
	v_pk_fma_f32 v[174:175], v[138:139], v[18:19], v[174:175]
	v_pk_fma_f32 v[176:177], v[140:141], v[16:17], v[176:177]
	v_cvt_pk_bf16_f32 v170, v170, v171
	v_cvt_pk_bf16_f32 v171, v172, v173
	v_cvt_pk_bf16_f32 v172, v174, v175
	v_cvt_pk_bf16_f32 v173, v176, v177
	s_mov_b64 s[34:35], 0x10000
	v_lshl_add_u64 v[188:189], v[32:33], 0, s[34:35]
	global_store_dwordx4 v[188:189], v[170:173], off
	s_nop 1
	s_waitcnt vmcnt(15)
; __device__ __forceinline__ unsigned cvt_pk_bf16(float lo, float hi) { unsigned r; asm volatile("v_cvt_pk_bf16_f32 %0, %1, %2" : "=v"(r) : "v"(lo), "v"(hi)); return r; }
;     __device__ __forceinline__ void operator()(const f32x4 (&acc)[2][2][4][2], const Unit& u, int wr, int wc, int fr, int fq) const {
;     ...
;                 for (int m = 0; m < 4; ++m) { const int row = row0 + ai * HALF + m * 16; const bf16_t* rp = resb + (size_t)row * D + col0; bf16_t* xp = X + (size_t)row * D + col0;
; #pragma unroll
;                     for (int bj = 0; bj < 2; ++bj) { const u32x4 r = *(const u32x4*)(rp + bj * HALF);
;                         const f32x4 v0 = (f32x4){bflo(r.x), bfhi(r.x), bflo(r.y), bfhi(r.y)} + gv[bj][0] * acc[ai][bj][m][0], v1 = (f32x4){bflo(r.z), bfhi(r.z), bflo(r.w), bfhi(r.w)} + gv[bj][1] * acc[ai][bj][m][1];
;                         u32x4 o; o.x = cvt_pk_bf16(v0[0], v0[1]); o.y = cvt_pk_bf16(v0[2], v0[3]); o.z = cvt_pk_bf16(v1[0], v1[1]); o.w = cvt_pk_bf16(v1[2], v1[3]);
;                         *(u32x4*)(xp + bj * HALF) = o; } }
	v_lshlrev_b32_e32 v170, 16, v204
	v_and_b32_e32 v171, 0xffff0000, v204
	v_lshlrev_b32_e32 v172, 16, v205
	v_and_b32_e32 v173, 0xffff0000, v205
	v_lshlrev_b32_e32 v174, 16, v206
	v_and_b32_e32 v175, 0xffff0000, v206
	v_lshlrev_b32_e32 v176, 16, v207
	v_and_b32_e32 v177, 0xffff0000, v207
	v_pk_fma_f32 v[170:171], v[134:135], v[14:15], v[170:171]
	v_pk_fma_f32 v[172:173], v[136:137], v[12:13], v[172:173]
	v_pk_fma_f32 v[174:175], v[130:131], v[10:11], v[174:175]
	v_pk_fma_f32 v[176:177], v[132:133], v[8:9], v[176:177]
	v_cvt_pk_bf16_f32 v170, v170, v171
	v_cvt_pk_bf16_f32 v171, v172, v173
	v_cvt_pk_bf16_f32 v172, v174, v175
	v_cvt_pk_bf16_f32 v173, v176, v177
	global_store_dwordx4 v[188:189], v[170:173], off offset:256
	s_nop 1
	s_waitcnt vmcnt(15)
	v_lshlrev_b32_e32 v170, 16, v208
	v_and_b32_e32 v171, 0xffff0000, v208
	v_lshlrev_b32_e32 v172, 16, v209
	v_and_b32_e32 v173, 0xffff0000, v209
	v_lshlrev_b32_e32 v174, 16, v210
	v_and_b32_e32 v175, 0xffff0000, v210
	v_lshlrev_b32_e32 v176, 16, v211
	v_and_b32_e32 v177, 0xffff0000, v211
	v_pk_fma_f32 v[170:171], v[126:127], v[22:23], v[170:171]
	v_pk_fma_f32 v[172:173], v[128:129], v[20:21], v[172:173]
	v_pk_fma_f32 v[174:175], v[122:123], v[18:19], v[174:175]
	v_pk_fma_f32 v[176:177], v[124:125], v[16:17], v[176:177]
	v_cvt_pk_bf16_f32 v170, v170, v171
	v_cvt_pk_bf16_f32 v171, v172, v173
	v_cvt_pk_bf16_f32 v172, v174, v175
	v_cvt_pk_bf16_f32 v173, v176, v177
	s_mov_b64 s[34:35], 0x20000
	v_lshl_add_u64 v[188:189], v[32:33], 0, s[34:35]
	global_store_dwordx4 v[188:189], v[170:173], off
	s_nop 1
	s_waitcnt vmcnt(15)
	v_lshlrev_b32_e32 v170, 16, v212
	v_and_b32_e32 v171, 0xffff0000, v212
	v_lshlrev_b32_e32 v172, 16, v213
	v_and_b32_e32 v173, 0xffff0000, v213
	v_lshlrev_b32_e32 v174, 16, v214
	v_and_b32_e32 v175, 0xffff0000, v214
	v_lshlrev_b32_e32 v176, 16, v215
	v_and_b32_e32 v177, 0xffff0000, v215
	v_pk_fma_f32 v[170:171], v[118:119], v[14:15], v[170:171]
	v_pk_fma_f32 v[172:173], v[120:121], v[12:13], v[172:173]
	v_pk_fma_f32 v[174:175], v[114:115], v[10:11], v[174:175]
	v_pk_fma_f32 v[176:177], v[116:117], v[8:9], v[176:177]
	v_cvt_pk_bf16_f32 v170, v170, v171
	v_cvt_pk_bf16_f32 v171, v172, v173
	v_cvt_pk_bf16_f32 v172, v174, v175
	v_cvt_pk_bf16_f32 v173, v176, v177
	global_store_dwordx4 v[188:189], v[170:173], off offset:256
	s_nop 1
	s_waitcnt vmcnt(15)
	v_lshlrev_b32_e32 v170, 16, v216
	v_and_b32_e32 v171, 0xffff0000, v216
	v_lshlrev_b32_e32 v172, 16, v217
	v_and_b32_e32 v173, 0xffff0000, v217
	v_lshlrev_b32_e32 v174, 16, v218
	v_and_b32_e32 v175, 0xffff0000, v218
	v_lshlrev_b32_e32 v176, 16, v219
	v_and_b32_e32 v177, 0xffff0000, v219
	v_pk_fma_f32 v[170:171], v[110:111], v[22:23], v[170:171]
	v_pk_fma_f32 v[172:173], v[112:113], v[20:21], v[172:173]
	v_pk_fma_f32 v[174:175], v[106:107], v[18:19], v[174:175]
	v_pk_fma_f32 v[176:177], v[108:109], v[16:17], v[176:177]
	v_cvt_pk_bf16_f32 v170, v170, v171
	v_cvt_pk_bf16_f32 v171, v172, v173
	v_cvt_pk_bf16_f32 v172, v174, v175
	v_cvt_pk_bf16_f32 v173, v176, v177
	s_mov_b64 s[34:35], 0x30000
	v_lshl_add_u64 v[188:189], v[32:33], 0, s[34:35]
	global_store_dwordx4 v[188:189], v[170:173], off
	s_nop 1
	s_waitcnt vmcnt(15)
	v_lshlrev_b32_e32 v170, 16, v220
	v_and_b32_e32 v171, 0xffff0000, v220
	v_lshlrev_b32_e32 v172, 16, v221
	v_and_b32_e32 v173, 0xffff0000, v221
	v_lshlrev_b32_e32 v174, 16, v222
	v_and_b32_e32 v175, 0xffff0000, v222
	v_lshlrev_b32_e32 v176, 16, v223
	v_and_b32_e32 v177, 0xffff0000, v223
	v_pk_fma_f32 v[170:171], v[102:103], v[14:15], v[170:171]
	v_pk_fma_f32 v[172:173], v[104:105], v[12:13], v[172:173]
	v_pk_fma_f32 v[174:175], v[98:99], v[10:11], v[174:175]
	v_pk_fma_f32 v[176:177], v[100:101], v[8:9], v[176:177]
	v_cvt_pk_bf16_f32 v170, v170, v171
	v_cvt_pk_bf16_f32 v171, v172, v173
	v_cvt_pk_bf16_f32 v172, v174, v175
	v_cvt_pk_bf16_f32 v173, v176, v177
	global_store_dwordx4 v[188:189], v[170:173], off offset:256
	s_nop 1
	s_waitcnt vmcnt(15)
	v_lshlrev_b32_e32 v170, 16, v242
	v_and_b32_e32 v171, 0xffff0000, v242
	v_lshlrev_b32_e32 v172, 16, v243
	v_and_b32_e32 v173, 0xffff0000, v243
	v_lshlrev_b32_e32 v174, 16, v244
	v_and_b32_e32 v175, 0xffff0000, v244
	v_lshlrev_b32_e32 v176, 16, v245
	v_and_b32_e32 v177, 0xffff0000, v245
	v_pk_fma_f32 v[170:171], v[94:95], v[22:23], v[170:171]
	v_pk_fma_f32 v[172:173], v[96:97], v[20:21], v[172:173]
	v_pk_fma_f32 v[174:175], v[90:91], v[18:19], v[174:175]
	v_pk_fma_f32 v[176:177], v[92:93], v[16:17], v[176:177]
	v_cvt_pk_bf16_f32 v170, v170, v171
	v_cvt_pk_bf16_f32 v171, v172, v173
	v_cvt_pk_bf16_f32 v172, v174, v175
	v_cvt_pk_bf16_f32 v173, v176, v177
	s_mov_b64 s[34:35], 0x80000
	v_lshl_add_u64 v[188:189], v[32:33], 0, s[34:35]
	global_store_dwordx4 v[188:189], v[170:173], off
	s_nop 1
	s_waitcnt vmcnt(15)
	v_lshlrev_b32_e32 v170, 16, v246
	v_and_b32_e32 v171, 0xffff0000, v246
	v_lshlrev_b32_e32 v172, 16, v247
	v_and_b32_e32 v173, 0xffff0000, v247
	v_lshlrev_b32_e32 v174, 16, v248
	v_and_b32_e32 v175, 0xffff0000, v248
	v_lshlrev_b32_e32 v176, 16, v249
	v_and_b32_e32 v177, 0xffff0000, v249
	v_pk_fma_f32 v[170:171], v[86:87], v[14:15], v[170:171]
	v_pk_fma_f32 v[172:173], v[88:89], v[12:13], v[172:173]
	v_pk_fma_f32 v[174:175], v[82:83], v[10:11], v[174:175]
	v_pk_fma_f32 v[176:177], v[84:85], v[8:9], v[176:177]
	v_cvt_pk_bf16_f32 v170, v170, v171
	v_cvt_pk_bf16_f32 v171, v172, v173
	v_cvt_pk_bf16_f32 v172, v174, v175
	v_cvt_pk_bf16_f32 v173, v176, v177
	global_store_dwordx4 v[188:189], v[170:173], off offset:256
	s_nop 1
	s_waitcnt vmcnt(14)
; __device__ __forceinline__ unsigned cvt_pk_bf16(float lo, float hi) { unsigned r; asm volatile("v_cvt_pk_bf16_f32 %0, %1, %2" : "=v"(r) : "v"(lo), "v"(hi)); return r; }
;     __device__ __forceinline__ void operator()(const f32x4 (&acc)[2][2][4][2], const Unit& u, int wr, int wc, int fr, int fq) const {
;     ...
;                 for (int m = 0; m < 4; ++m) { const int row = row0 + ai * HALF + m * 16; const bf16_t* rp = resb + (size_t)row * D + col0; bf16_t* xp = X + (size_t)row * D + col0;
; #pragma unroll
;                     for (int bj = 0; bj < 2; ++bj) { const u32x4 r = *(const u32x4*)(rp + bj * HALF);
;                         const f32x4 v0 = (f32x4){bflo(r.x), bfhi(r.x), bflo(r.y), bfhi(r.y)} + gv[bj][0] * acc[ai][bj][m][0], v1 = (f32x4){bflo(r.z), bfhi(r.z), bflo(r.w), bfhi(r.w)} + gv[bj][1] * acc[ai][bj][m][1];
;                         u32x4 o; o.x = cvt_pk_bf16(v0[0], v0[1]); o.y = cvt_pk_bf16(v0[2], v0[3]); o.z = cvt_pk_bf16(v1[0], v1[1]); o.w = cvt_pk_bf16(v1[2], v1[3]);
;                         *(u32x4*)(xp + bj * HALF) = o; } }
	v_lshlrev_b32_e32 v170, 16, v190
	v_and_b32_e32 v171, 0xffff0000, v190
	v_lshlrev_b32_e32 v172, 16, v191
	v_and_b32_e32 v173, 0xffff0000, v191
	v_lshlrev_b32_e32 v174, 16, v192
	v_and_b32_e32 v175, 0xffff0000, v192
	v_lshlrev_b32_e32 v176, 16, v193
	v_and_b32_e32 v177, 0xffff0000, v193
	v_pk_fma_f32 v[170:171], v[78:79], v[22:23], v[170:171]
	v_pk_fma_f32 v[172:173], v[80:81], v[20:21], v[172:173]
	v_pk_fma_f32 v[174:175], v[74:75], v[18:19], v[174:175]
	v_pk_fma_f32 v[176:177], v[76:77], v[16:17], v[176:177]
	v_cvt_pk_bf16_f32 v170, v170, v171
	v_cvt_pk_bf16_f32 v171, v172, v173
	v_cvt_pk_bf16_f32 v172, v174, v175
	v_cvt_pk_bf16_f32 v173, v176, v177
	s_mov_b64 s[34:35], 0x90000
	v_lshl_add_u64 v[188:189], v[32:33], 0, s[34:35]
	global_store_dwordx4 v[188:189], v[170:173], off
	s_nop 1
	s_waitcnt vmcnt(14)
	v_lshlrev_b32_e32 v170, 16, v158
	v_and_b32_e32 v171, 0xffff0000, v158
	v_lshlrev_b32_e32 v172, 16, v159
	v_and_b32_e32 v173, 0xffff0000, v159
	v_lshlrev_b32_e32 v174, 16, v160
	v_and_b32_e32 v175, 0xffff0000, v160
	v_lshlrev_b32_e32 v176, 16, v161
	v_and_b32_e32 v177, 0xffff0000, v161
	v_pk_fma_f32 v[170:171], v[70:71], v[14:15], v[170:171]
	v_pk_fma_f32 v[172:173], v[72:73], v[12:13], v[172:173]
	v_pk_fma_f32 v[174:175], v[66:67], v[10:11], v[174:175]
	v_pk_fma_f32 v[176:177], v[68:69], v[8:9], v[176:177]
	v_cvt_pk_bf16_f32 v170, v170, v171
	v_cvt_pk_bf16_f32 v171, v172, v173
	v_cvt_pk_bf16_f32 v172, v174, v175
	v_cvt_pk_bf16_f32 v173, v176, v177
	global_store_dwordx4 v[188:189], v[170:173], off offset:256
	s_nop 1
	s_waitcnt vmcnt(14)
	v_lshlrev_b32_e32 v170, 16, v154
	v_and_b32_e32 v171, 0xffff0000, v154
	v_lshlrev_b32_e32 v172, 16, v155
	v_and_b32_e32 v173, 0xffff0000, v155
	v_lshlrev_b32_e32 v174, 16, v156
	v_and_b32_e32 v175, 0xffff0000, v156
	v_lshlrev_b32_e32 v176, 16, v157
	v_and_b32_e32 v177, 0xffff0000, v157
	v_pk_fma_f32 v[170:171], v[62:63], v[22:23], v[170:171]
	v_pk_fma_f32 v[172:173], v[64:65], v[20:21], v[172:173]
	v_pk_fma_f32 v[174:175], v[58:59], v[18:19], v[174:175]
	v_pk_fma_f32 v[176:177], v[60:61], v[16:17], v[176:177]
	v_cvt_pk_bf16_f32 v170, v170, v171
	v_cvt_pk_bf16_f32 v171, v172, v173
	v_cvt_pk_bf16_f32 v172, v174, v175
	v_cvt_pk_bf16_f32 v173, v176, v177
	s_mov_b64 s[34:35], 0xa0000
	v_lshl_add_u64 v[188:189], v[32:33], 0, s[34:35]
	global_store_dwordx4 v[188:189], v[170:173], off
	s_nop 1
	s_waitcnt vmcnt(13)
	v_lshlrev_b32_e32 v170, 16, v196
	v_and_b32_e32 v171, 0xffff0000, v196
	v_lshlrev_b32_e32 v172, 16, v197
	v_and_b32_e32 v173, 0xffff0000, v197
	v_lshlrev_b32_e32 v174, 16, v198
	v_and_b32_e32 v175, 0xffff0000, v198
	v_lshlrev_b32_e32 v176, 16, v199
	v_and_b32_e32 v177, 0xffff0000, v199
	v_pk_fma_f32 v[170:171], v[54:55], v[14:15], v[170:171]
	v_pk_fma_f32 v[172:173], v[56:57], v[12:13], v[172:173]
	v_pk_fma_f32 v[174:175], v[50:51], v[10:11], v[174:175]
	v_pk_fma_f32 v[176:177], v[52:53], v[8:9], v[176:177]
	v_cvt_pk_bf16_f32 v170, v170, v171
	v_cvt_pk_bf16_f32 v171, v172, v173
	v_cvt_pk_bf16_f32 v172, v174, v175
	v_cvt_pk_bf16_f32 v173, v176, v177
	global_store_dwordx4 v[188:189], v[170:173], off offset:256
	s_nop 1
	s_waitcnt vmcnt(13)
	v_lshlrev_b32_e32 v170, 16, v150
	v_and_b32_e32 v171, 0xffff0000, v150
	v_lshlrev_b32_e32 v172, 16, v151
	v_and_b32_e32 v173, 0xffff0000, v151
	v_lshlrev_b32_e32 v174, 16, v152
	v_and_b32_e32 v175, 0xffff0000, v152
	v_lshlrev_b32_e32 v176, 16, v153
	v_and_b32_e32 v177, 0xffff0000, v153
	v_pk_fma_f32 v[170:171], v[46:47], v[22:23], v[170:171]
	v_pk_fma_f32 v[172:173], v[48:49], v[20:21], v[172:173]
	v_pk_fma_f32 v[174:175], v[42:43], v[18:19], v[174:175]
	v_pk_fma_f32 v[176:177], v[44:45], v[16:17], v[176:177]
	v_cvt_pk_bf16_f32 v170, v170, v171
	v_cvt_pk_bf16_f32 v171, v172, v173
	v_cvt_pk_bf16_f32 v172, v174, v175
	v_cvt_pk_bf16_f32 v173, v176, v177
	s_mov_b64 s[34:35], 0xb0000
	v_lshl_add_u64 v[188:189], v[32:33], 0, s[34:35]
	global_store_dwordx4 v[188:189], v[170:173], off
	s_nop 1
	s_waitcnt vmcnt(13)
	v_lshlrev_b32_e32 v170, 16, v146
	v_and_b32_e32 v171, 0xffff0000, v146
	v_lshlrev_b32_e32 v172, 16, v147
	v_and_b32_e32 v173, 0xffff0000, v147
	v_lshlrev_b32_e32 v174, 16, v148
	v_and_b32_e32 v175, 0xffff0000, v148
	v_lshlrev_b32_e32 v176, 16, v149
	v_and_b32_e32 v177, 0xffff0000, v149
	v_pk_fma_f32 v[170:171], v[38:39], v[14:15], v[170:171]
	v_pk_fma_f32 v[172:173], v[40:41], v[12:13], v[172:173]
	v_pk_fma_f32 v[174:175], v[34:35], v[10:11], v[174:175]
	v_pk_fma_f32 v[176:177], v[36:37], v[8:9], v[176:177]
	s_mov_b64 s[34:35], 0xb0000
	v_lshl_add_u64 v[32:33], v[186:187], 0, s[34:35]
	v_cvt_pk_bf16_f32 v2, v170, v171
	v_cvt_pk_bf16_f32 v3, v172, v173
	v_cvt_pk_bf16_f32 v4, v174, v175
	v_cvt_pk_bf16_f32 v5, v176, v177
	s_mov_b64 s[34:35], 0
; __device__ __forceinline__ unsigned cvt_pk_bf16(float lo, float hi) { unsigned r; asm volatile("v_cvt_pk_bf16_f32 %0, %1, %2" : "=v"(r) : "v"(lo), "v"(hi)); return r; }
;     __device__ __forceinline__ void operator()(const f32x4 (&acc)[2][2][4][2], const Unit& u, int wr, int wc, int fr, int fq) const {
;     ...
;             for (int ai = 0; ai < 2; ++ai)
; #pragma unroll
;                 for (int m = 0; m < 4; ++m) { const int row = row0 + ai * HALF + m * 16;
;                     const float* rp = (row < TL ? res_lat + (size_t)row * D : res_ctx + (size_t)(row - TL) * D) + col0; bf16_t* xp = X + (size_t)row * D + col0;
; #pragma unroll
;                     for (int bj = 0; bj < 2; ++bj) { const f32x4 r0 = *(const f32x4*)(rp + bj * HALF), r1 = *(const f32x4*)(rp + bj * HALF + 4);
;                         const f32x4 v0 = r0 + gv[bj][0] * acc[ai][bj][m][0], v1 = r1 + gv[bj][1] * acc[ai][bj][m][1];
;                         u32x4 o; o.x = cvt_pk_bf16(v0[0], v0[1]); o.y = cvt_pk_bf16(v0[2], v0[3]); o.z = cvt_pk_bf16(v1[0], v1[1]); o.w = cvt_pk_bf16(v1[2], v1[3]);
;                         *(u32x4*)(xp + bj * HALF) = o; } }
.LBB0_925:
	s_andn2_b64 vcc, exec, s[34:35]
	v_readlane_b32 s90, v254, 28
	v_readlane_b32 s89, v254, 30
	v_readlane_b32 s91, v254, 29
	s_cbranch_vccnz .LBB0_959
	v_ashrrev_i32_e32 v25, 31, v24
	v_lshlrev_b64 v[186:187], 12, v[24:25]
	v_lshl_add_u64 v[32:33], s[38:39], 0, v[186:187]
	v_lshl_add_u64 v[32:33], v[6:7], 1, v[32:33]
	v_lshlrev_b64 v[2:3], 13, v[24:25]
	v_lshl_add_u64 v[2:3], s[8:9], 0, v[2:3]
	v_add_u32_e32 v4, 0xffffc000, v24
	v_mov_b32_e32 v5, v0
	v_lshlrev_b64 v[4:5], 13, v[4:5]
	v_lshl_add_u64 v[4:5], s[16:17], 0, v[4:5]
	s_movk_i32 s34, 0x3fff
	v_cmp_lt_i32_e32 vcc, s34, v24
	s_nop 1
	v_cndmask_b32_e32 v2, v2, v4, vcc
	v_cndmask_b32_e32 v3, v3, v5, vcc
	v_lshl_add_u64 v[30:31], v[6:7], 2, v[2:3]
	global_load_dwordx4 v[190:193], v[30:31], off nt
	global_load_dwordx4 v[196:199], v[30:31], off offset:16 nt
	global_load_dwordx4 v[200:203], v[30:31], off offset:512 nt
	global_load_dwordx4 v[204:207], v[30:31], off offset:528 nt
	s_mov_b64 s[34:35], 0x20000
	v_lshl_add_u64 v[184:185], v[30:31], 0, s[34:35]
	global_load_dwordx4 v[208:211], v[184:185], off nt
	global_load_dwordx4 v[212:215], v[184:185], off offset:16 nt
	global_load_dwordx4 v[216:219], v[184:185], off offset:512 nt
	global_load_dwordx4 v[220:223], v[184:185], off offset:528 nt
	s_mov_b64 s[34:35], 0x40000
	v_lshl_add_u64 v[184:185], v[30:31], 0, s[34:35]
	global_load_dwordx4 v[242:245], v[184:185], off nt
	global_load_dwordx4 v[246:249], v[184:185], off offset:16 nt
	s_waitcnt vmcnt(8)
	v_pk_fma_f32 v[170:171], v[158:159], v[22:23], v[190:191]
	v_pk_fma_f32 v[172:173], v[160:161], v[20:21], v[192:193]
	v_pk_fma_f32 v[174:175], v[154:155], v[18:19], v[196:197]
	v_pk_fma_f32 v[176:177], v[156:157], v[16:17], v[198:199]
	v_cvt_pk_bf16_f32 v170, v170, v171
	v_cvt_pk_bf16_f32 v171, v172, v173
	v_cvt_pk_bf16_f32 v172, v174, v175
	v_cvt_pk_bf16_f32 v173, v176, v177
	global_store_dwordx4 v[32:33], v[170:173], off
	s_nop 1
	global_load_dwordx4 v[190:193], v[184:185], off offset:512 nt
	global_load_dwordx4 v[196:199], v[184:185], off offset:528 nt
	s_mov_b64 s[34:35], 0x60000
	v_lshl_add_u64 v[184:185], v[30:31], 0, s[34:35]
	global_load_dwordx4 v[158:161], v[184:185], off nt
	global_load_dwordx4 v[154:157], v[184:185], off offset:16 nt
	s_waitcnt vmcnt(11)
	v_pk_fma_f32 v[170:171], v[150:151], v[14:15], v[200:201]
	v_pk_fma_f32 v[172:173], v[152:153], v[12:13], v[202:203]
	v_pk_fma_f32 v[174:175], v[146:147], v[10:11], v[204:205]
	v_pk_fma_f32 v[176:177], v[148:149], v[8:9], v[206:207]
	v_cvt_pk_bf16_f32 v170, v170, v171
	v_cvt_pk_bf16_f32 v171, v172, v173
	v_cvt_pk_bf16_f32 v172, v174, v175
	v_cvt_pk_bf16_f32 v173, v176, v177
	global_store_dwordx4 v[32:33], v[170:173], off offset:256
	s_nop 1
	global_load_dwordx4 v[200:203], v[184:185], off offset:512 nt
	global_load_dwordx4 v[204:207], v[184:185], off offset:528 nt
	s_mov_b64 s[34:35], 0x100000
	v_lshl_add_u64 v[184:185], v[30:31], 0, s[34:35]
	global_load_dwordx4 v[150:153], v[184:185], off nt
	global_load_dwordx4 v[146:149], v[184:185], off offset:16 nt
	s_waitcnt vmcnt(14)
	v_pk_fma_f32 v[170:171], v[142:143], v[22:23], v[208:209]
	v_pk_fma_f32 v[172:173], v[144:145], v[20:21], v[210:211]
	v_pk_fma_f32 v[174:175], v[138:139], v[18:19], v[212:213]
	v_pk_fma_f32 v[176:177], v[140:141], v[16:17], v[214:215]
	v_cvt_pk_bf16_f32 v170, v170, v171
	v_cvt_pk_bf16_f32 v171, v172, v173
	v_cvt_pk_bf16_f32 v172, v174, v175
	v_cvt_pk_bf16_f32 v173, v176, v177
	s_mov_b64 s[34:35], 0x10000
	v_lshl_add_u64 v[188:189], v[32:33], 0, s[34:35]
	global_store_dwordx4 v[188:189], v[170:173], off
	s_nop 1
	global_load_dwordx4 v[208:211], v[184:185], off offset:512 nt
	global_load_dwordx4 v[212:215], v[184:185], off offset:528 nt
	s_mov_b64 s[34:35], 0x120000
	v_lshl_add_u64 v[184:185], v[30:31], 0, s[34:35]
	global_load_dwordx4 v[142:145], v[184:185], off nt
	global_load_dwordx4 v[138:141], v[184:185], off offset:16 nt
	s_waitcnt vmcnt(17)
	v_pk_fma_f32 v[170:171], v[134:135], v[14:15], v[216:217]
	v_pk_fma_f32 v[172:173], v[136:137], v[12:13], v[218:219]
	v_pk_fma_f32 v[174:175], v[130:131], v[10:11], v[220:221]
	v_pk_fma_f32 v[176:177], v[132:133], v[8:9], v[222:223]
	v_cvt_pk_bf16_f32 v170, v170, v171
	v_cvt_pk_bf16_f32 v171, v172, v173
	v_cvt_pk_bf16_f32 v172, v174, v175
	v_cvt_pk_bf16_f32 v173, v176, v177
	global_store_dwordx4 v[188:189], v[170:173], off offset:256
	s_nop 1
	global_load_dwordx4 v[216:219], v[184:185], off offset:512 nt
	global_load_dwordx4 v[220:223], v[184:185], off offset:528 nt
	s_mov_b64 s[34:35], 0x140000
	v_lshl_add_u64 v[184:185], v[30:31], 0, s[34:35]
	global_load_dwordx4 v[134:137], v[184:185], off nt
	global_load_dwordx4 v[130:133], v[184:185], off offset:16 nt
	s_waitcnt vmcnt(20)
	v_pk_fma_f32 v[170:171], v[126:127], v[22:23], v[242:243]
	v_pk_fma_f32 v[172:173], v[128:129], v[20:21], v[244:245]
	v_pk_fma_f32 v[174:175], v[122:123], v[18:19], v[246:247]
	v_pk_fma_f32 v[176:177], v[124:125], v[16:17], v[248:249]
	v_cvt_pk_bf16_f32 v170, v170, v171
	v_cvt_pk_bf16_f32 v171, v172, v173
	v_cvt_pk_bf16_f32 v172, v174, v175
	v_cvt_pk_bf16_f32 v173, v176, v177
	s_mov_b64 s[34:35], 0x20000
	v_lshl_add_u64 v[188:189], v[32:33], 0, s[34:35]
	global_store_dwordx4 v[188:189], v[170:173], off
	s_nop 1
	global_load_dwordx4 v[242:245], v[184:185], off offset:512 nt
	global_load_dwordx4 v[246:249], v[184:185], off offset:528 nt
	s_mov_b64 s[34:35], 0x160000
	v_lshl_add_u64 v[184:185], v[30:31], 0, s[34:35]
	global_load_dwordx4 v[126:129], v[184:185], off nt
	global_load_dwordx4 v[122:125], v[184:185], off offset:16 nt
	s_waitcnt vmcnt(22)
; __device__ __forceinline__ unsigned cvt_pk_bf16(float lo, float hi) { unsigned r; asm volatile("v_cvt_pk_bf16_f32 %0, %1, %2" : "=v"(r) : "v"(lo), "v"(hi)); return r; }
;     __device__ __forceinline__ void operator()(const f32x4 (&acc)[2][2][4][2], const Unit& u, int wr, int wc, int fr, int fq) const {
;     ...
;             for (int ai = 0; ai < 2; ++ai)
; #pragma unroll
;                 for (int m = 0; m < 4; ++m) { const int row = row0 + ai * HALF + m * 16;
;                     const float* rp = (row < TL ? res_lat + (size_t)row * D : res_ctx + (size_t)(row - TL) * D) + col0; bf16_t* xp = X + (size_t)row * D + col0;
; #pragma unroll
;                     for (int bj = 0; bj < 2; ++bj) { const f32x4 r0 = *(const f32x4*)(rp + bj * HALF), r1 = *(const f32x4*)(rp + bj * HALF + 4);
;                         const f32x4 v0 = r0 + gv[bj][0] * acc[ai][bj][m][0], v1 = r1 + gv[bj][1] * acc[ai][bj][m][1];
;                         u32x4 o; o.x = cvt_pk_bf16(v0[0], v0[1]); o.y = cvt_pk_bf16(v0[2], v0[3]); o.z = cvt_pk_bf16(v1[0], v1[1]); o.w = cvt_pk_bf16(v1[2], v1[3]);
;                         *(u32x4*)(xp + bj * HALF) = o; } }
	v_pk_fma_f32 v[170:171], v[118:119], v[14:15], v[190:191]
	v_pk_fma_f32 v[172:173], v[120:121], v[12:13], v[192:193]
	v_pk_fma_f32 v[174:175], v[114:115], v[10:11], v[196:197]
	v_pk_fma_f32 v[176:177], v[116:117], v[8:9], v[198:199]
	v_cvt_pk_bf16_f32 v170, v170, v171
	v_cvt_pk_bf16_f32 v171, v172, v173
	v_cvt_pk_bf16_f32 v172, v174, v175
	v_cvt_pk_bf16_f32 v173, v176, v177
	global_store_dwordx4 v[188:189], v[170:173], off offset:256
	s_nop 1
	global_load_dwordx4 v[190:193], v[184:185], off offset:512 nt
	global_load_dwordx4 v[196:199], v[184:185], off offset:528 nt
	s_waitcnt vmcnt(23)
	v_pk_fma_f32 v[170:171], v[110:111], v[22:23], v[158:159]
	v_pk_fma_f32 v[172:173], v[112:113], v[20:21], v[160:161]
	v_pk_fma_f32 v[174:175], v[106:107], v[18:19], v[154:155]
	v_pk_fma_f32 v[176:177], v[108:109], v[16:17], v[156:157]
	v_cvt_pk_bf16_f32 v170, v170, v171
	v_cvt_pk_bf16_f32 v171, v172, v173
	v_cvt_pk_bf16_f32 v172, v174, v175
	v_cvt_pk_bf16_f32 v173, v176, v177
	s_mov_b64 s[34:35], 0x30000
	v_lshl_add_u64 v[188:189], v[32:33], 0, s[34:35]
	global_store_dwordx4 v[188:189], v[170:173], off
	s_nop 1
	s_waitcnt vmcnt(21)
	v_pk_fma_f32 v[170:171], v[102:103], v[14:15], v[200:201]
	v_pk_fma_f32 v[172:173], v[104:105], v[12:13], v[202:203]
	v_pk_fma_f32 v[174:175], v[98:99], v[10:11], v[204:205]
	v_pk_fma_f32 v[176:177], v[100:101], v[8:9], v[206:207]
	v_cvt_pk_bf16_f32 v170, v170, v171
	v_cvt_pk_bf16_f32 v171, v172, v173
	v_cvt_pk_bf16_f32 v172, v174, v175
	v_cvt_pk_bf16_f32 v173, v176, v177
	global_store_dwordx4 v[188:189], v[170:173], off offset:256
	s_nop 1
	s_waitcnt vmcnt(20)
	v_pk_fma_f32 v[170:171], v[94:95], v[22:23], v[150:151]
	v_pk_fma_f32 v[172:173], v[96:97], v[20:21], v[152:153]
	v_pk_fma_f32 v[174:175], v[90:91], v[18:19], v[146:147]
	v_pk_fma_f32 v[176:177], v[92:93], v[16:17], v[148:149]
	v_cvt_pk_bf16_f32 v170, v170, v171
	v_cvt_pk_bf16_f32 v171, v172, v173
	v_cvt_pk_bf16_f32 v172, v174, v175
	v_cvt_pk_bf16_f32 v173, v176, v177
	s_mov_b64 s[34:35], 0x80000
	v_lshl_add_u64 v[188:189], v[32:33], 0, s[34:35]
	global_store_dwordx4 v[188:189], v[170:173], off
	s_nop 1
	s_waitcnt vmcnt(18)
	v_pk_fma_f32 v[170:171], v[86:87], v[14:15], v[208:209]
	v_pk_fma_f32 v[172:173], v[88:89], v[12:13], v[210:211]
	v_pk_fma_f32 v[174:175], v[82:83], v[10:11], v[212:213]
	v_pk_fma_f32 v[176:177], v[84:85], v[8:9], v[214:215]
	v_cvt_pk_bf16_f32 v170, v170, v171
	v_cvt_pk_bf16_f32 v171, v172, v173
	v_cvt_pk_bf16_f32 v172, v174, v175
	v_cvt_pk_bf16_f32 v173, v176, v177
	global_store_dwordx4 v[188:189], v[170:173], off offset:256
	s_nop 1
	s_waitcnt vmcnt(17)
	v_pk_fma_f32 v[170:171], v[78:79], v[22:23], v[142:143]
	v_pk_fma_f32 v[172:173], v[80:81], v[20:21], v[144:145]
	v_pk_fma_f32 v[174:175], v[74:75], v[18:19], v[138:139]
	v_pk_fma_f32 v[176:177], v[76:77], v[16:17], v[140:141]
	v_cvt_pk_bf16_f32 v170, v170, v171
	v_cvt_pk_bf16_f32 v171, v172, v173
	v_cvt_pk_bf16_f32 v172, v174, v175
	v_cvt_pk_bf16_f32 v173, v176, v177
	s_mov_b64 s[34:35], 0x90000
	v_lshl_add_u64 v[188:189], v[32:33], 0, s[34:35]
	global_store_dwordx4 v[188:189], v[170:173], off
	s_nop 1
	s_waitcnt vmcnt(15)
	v_pk_fma_f32 v[170:171], v[70:71], v[14:15], v[216:217]
	v_pk_fma_f32 v[172:173], v[72:73], v[12:13], v[218:219]
	v_pk_fma_f32 v[174:175], v[66:67], v[10:11], v[220:221]
	v_pk_fma_f32 v[176:177], v[68:69], v[8:9], v[222:223]
	v_cvt_pk_bf16_f32 v170, v170, v171
	v_cvt_pk_bf16_f32 v171, v172, v173
	v_cvt_pk_bf16_f32 v172, v174, v175
	v_cvt_pk_bf16_f32 v173, v176, v177
	global_store_dwordx4 v[188:189], v[170:173], off offset:256
	s_nop 1
	s_waitcnt vmcnt(14)
	v_pk_fma_f32 v[170:171], v[62:63], v[22:23], v[134:135]
	v_pk_fma_f32 v[172:173], v[64:65], v[20:21], v[136:137]
	v_pk_fma_f32 v[174:175], v[58:59], v[18:19], v[130:131]
	v_pk_fma_f32 v[176:177], v[60:61], v[16:17], v[132:133]
	v_cvt_pk_bf16_f32 v170, v170, v171
	v_cvt_pk_bf16_f32 v171, v172, v173
	v_cvt_pk_bf16_f32 v172, v174, v175
	v_cvt_pk_bf16_f32 v173, v176, v177
	s_mov_b64 s[34:35], 0xa0000
	v_lshl_add_u64 v[188:189], v[32:33], 0, s[34:35]
	global_store_dwordx4 v[188:189], v[170:173], off
	s_nop 1
	s_waitcnt vmcnt(12)
	v_pk_fma_f32 v[170:171], v[54:55], v[14:15], v[242:243]
	v_pk_fma_f32 v[172:173], v[56:57], v[12:13], v[244:245]
	v_pk_fma_f32 v[174:175], v[50:51], v[10:11], v[246:247]
	v_pk_fma_f32 v[176:177], v[52:53], v[8:9], v[248:249]
	v_cvt_pk_bf16_f32 v170, v170, v171
	v_cvt_pk_bf16_f32 v171, v172, v173
	v_cvt_pk_bf16_f32 v172, v174, v175
	v_cvt_pk_bf16_f32 v173, v176, v177
	global_store_dwordx4 v[188:189], v[170:173], off offset:256
	s_nop 1
	s_waitcnt vmcnt(11)
	v_pk_fma_f32 v[170:171], v[46:47], v[22:23], v[126:127]
	v_pk_fma_f32 v[172:173], v[48:49], v[20:21], v[128:129]
	v_pk_fma_f32 v[174:175], v[42:43], v[18:19], v[122:123]
	v_pk_fma_f32 v[176:177], v[44:45], v[16:17], v[124:125]
	v_cvt_pk_bf16_f32 v170, v170, v171
	v_cvt_pk_bf16_f32 v171, v172, v173
	v_cvt_pk_bf16_f32 v172, v174, v175
	v_cvt_pk_bf16_f32 v173, v176, v177
	s_mov_b64 s[34:35], 0xb0000
	v_lshl_add_u64 v[188:189], v[32:33], 0, s[34:35]
	global_store_dwordx4 v[188:189], v[170:173], off
	s_nop 1
	s_waitcnt vmcnt(9)
	v_pk_fma_f32 v[170:171], v[38:39], v[14:15], v[190:191]
	v_pk_fma_f32 v[172:173], v[40:41], v[12:13], v[192:193]
	v_pk_fma_f32 v[174:175], v[34:35], v[10:11], v[196:197]
	v_pk_fma_f32 v[176:177], v[36:37], v[8:9], v[198:199]
	s_mov_b64 s[34:35], 0xb0000
	v_lshl_add_u64 v[32:33], v[186:187], 0, s[34:35]
	v_cvt_pk_bf16_f32 v2, v170, v171
	v_cvt_pk_bf16_f32 v3, v172, v173
	v_cvt_pk_bf16_f32 v4, v174, v175
	v_cvt_pk_bf16_f32 v5, v176, v177
